# stick-breaking unit start waits only for the prefetched loads, not for the previous unit's output stores
# speedup vs baseline: 1.0025x; 1.0000x over previous
; #define LAS __attribute__((address_space(3)))
; __device__ __forceinline__ void sb_prefetch(bf16x8 (&qr)[4], int b, int hp, int u, const bf16_t* Q, const bf16_t* K, const bf16_t* V, LAS char* L, int wid, int lane) {
;     const int r32 = lane & 31, hi = lane >> 5; const int hh = wid >> 2, qw = wid & 3, h = 2 * hp + hh;
;     const int t0 = 128 * u + 32 * qw; const size_t rowbase = (size_t)b * T; const int jtop = 2 * u + 1;
;     const bf16_t* Qw = Q + (rowbase + t0) * D + h * 64; const bf16_t* Kh = K + rowbase * D + h * 64; const bf16_t* Vh = V + rowbase * D + h * 64;
;     const unsigned kvoff = (unsigned)lane * 2048u, vvoff = (unsigned)((lane >> 2) * D + (lane & 3) * 8) * 2u;
;     const int pa = 2 * qw, pb = 2 * qw + 1;
;     const bf16_t* Kwa = Kh + pa * 8; const bf16_t* Kwb = Kh + pb * 8;
;     const bf16_t* Vwa = Vh + (size_t)(16 * (pa & 3)) * D + (pa >> 2) * 32; const bf16_t* Vwb = Vh + (size_t)(16 * (pb & 3)) * D + (pb >> 2) * 32;
;     const unsigned hbase = (unsigned)(size_t)L + hh * SL_HEAD;
;     const unsigned kda = hbase + pa * 1024u, kdb = hbase + pb * 1024u, vda = hbase + SL_VOFF + pa * 1024u, vdb = hbase + SL_VOFF + pb * 1024u;
; #pragma unroll
;     for (int k = 0; k < 2; ++k) { const size_t ro_ = (size_t)(jtop - k) * 64 * D; const unsigned so_ = (unsigned)(k * SL_SLOT);
;         glds16_s(Kwa + ro_, kvoff, kda + so_); glds16_s(Kwb + ro_, kvoff, kdb + so_); glds16_s(Vwa + ro_, vvoff, vda + so_); glds16_s(Vwb + ro_, vvoff, vdb + so_); }
; #pragma unroll
;     for (int d0 = 0; d0 < 4; ++d0) qr[d0] = *(const bf16x8*)(Qw + (size_t)r32 * D + 16 * d0 + 8 * hi);
; }
; __global__ void __launch_bounds__(512, 2) trunk_fwd(Args args) {
;     ...
;               { bf16x8 qr[4]; int u = F.vcu;
;                 { const int u0 = u < NB * 8 * 32 ? u : 0;
;                   sb_prefetch(qr, u0 >> 8, (u0 >> 5) & 7, u0 & 31, (const bf16_t*)(ws + WS_OQ), (const bf16_t*)(ws + WS_OK), (const bf16_t*)(ws + WS_OV), (LAS char*)F.lds, F.wave, F.lane); }
;                 for (; u < NB * 8 * 32; u += F.G) { const int bh = u >> 5, ub = u & 31; const int un = u + F.G; const bool hn = un < NB * 8 * 32;
;                     sb_block_unit(qr, bh >> 3, bh & 7, ub, hn ? (un >> 8) : -1, (un >> 5) & 7, un & 31, (const bf16_t*)(ws + WS_OQ), (const bf16_t*)(ws + WS_OK), (const bf16_t*)(ws + WS_OV), (bf16_t*)(ws + WS_OQ), (LAS char*)F.lds, F.wave, F.lane); } } }
.LBB0_348:
	s_cmpk_lt_i32 s82, 0x400
	s_cselect_b32 s2, s82, 0
	s_ashr_i32 s0, s2, 8
	s_and_b32 s3, s2, 31
	s_load_dwordx2 s[6:7], s[76:77], 0x78
	s_waitcnt lgkmcnt(0)
	s_add_u32 s8, s6, 0xa700000
	s_addc_u32 s9, s7, 0
	s_add_u32 s10, s6, 0xc700000
	s_addc_u32 s11, s7, 0
	s_lshl_b32 s2, s2, 2
	s_ashr_i32 s1, s0, 31
	s_and_b32 s2, s2, 0x380
	v_readlane_b32 s4, v254, 3
	s_add_i32 s2, s2, s4
	s_lshl_b64 s[4:5], s[0:1], 23
	s_add_u32 s1, s8, s4
	v_writelane_b32 v255, s8, 10
	s_addc_u32 s8, s9, s5
	s_lshl_b32 s0, s2, 1
	s_add_u32 s1, s1, s0
	s_addc_u32 s2, s8, 0
	s_add_u32 s8, s10, s4
	v_writelane_b32 v255, s9, 11
	s_addc_u32 s9, s11, s5
	s_add_u32 s8, s8, s0
	v_writelane_b32 v255, s10, 12
	s_addc_u32 s9, s9, 0
	v_readlane_b32 s10, v254, 44
	s_add_u32 s14, s1, s10
	s_addc_u32 s15, s2, 0
	v_readlane_b32 s10, v254, 45
	s_add_u32 s16, s1, s10
	s_addc_u32 s17, s2, 0
	v_readlane_b32 s1, v254, 46
	s_add_u32 s1, s8, s1
	s_addc_u32 s2, s9, 0
	v_readlane_b32 s10, v254, 47
	s_add_u32 s18, s1, s10
	s_addc_u32 s19, s2, 0
	v_readlane_b32 s1, v254, 48
	s_add_u32 s1, s8, s1
	s_addc_u32 s2, s9, 0
	s_add_u32 s20, s1, s10
	s_addc_u32 s21, s2, 0
	s_lshl_b32 s1, s3, 18
	s_or_b32 s12, s1, 0x20000
	s_add_u32 s2, s14, s12
	s_addc_u32 s3, s15, 0
	s_add_u32 s8, s16, s12
	s_addc_u32 s9, s17, 0
	s_add_u32 s10, s18, s12
	v_writelane_b32 v255, s11, 13
	s_addc_u32 s11, s19, 0
	v_and_b32_e32 v2, 63, v3
	s_add_u32 s12, s20, s12
	s_addc_u32 s13, s21, 0
	v_lshlrev_b32_e32 v0, 9, v3
	s_waitcnt vmcnt(13)
	v_lshlrev_b32_e32 v4, 4, v2
	s_movk_i32 s22, 0x7830
	s_add_u32 s14, s14, s1
	v_lshlrev_b32_e32 v142, 11, v2
	v_bitop3_b32 v143, v0, s22, v4 bitop3:0xc8
	v_readlane_b32 s23, v254, 5
	s_nop 4
	s_mov_b32 s22, m0
	s_mov_b32 m0, s23
	s_nop 0
	global_load_lds_dwordx4 v142, s[2:3]
	s_mov_b32 m0, s22
	s_addc_u32 s15, s15, 0
	v_readlane_b32 s3, v254, 7
	s_nop 4
	s_mov_b32 s2, m0
	s_mov_b32 m0, s3
	s_nop 0
	global_load_lds_dwordx4 v142, s[8:9]
	s_mov_b32 m0, s2
	s_add_u32 s16, s16, s1
	v_readlane_b32 s3, v254, 9
	s_nop 4
	s_mov_b32 s2, m0
	s_mov_b32 m0, s3
	s_nop 0
	global_load_lds_dwordx4 v143, s[10:11]
	s_mov_b32 m0, s2
	s_addc_u32 s17, s17, 0
	v_readlane_b32 s3, v254, 11
	s_nop 4
	s_mov_b32 s2, m0
	s_mov_b32 m0, s3
	s_nop 0
	global_load_lds_dwordx4 v143, s[12:13]
	s_mov_b32 m0, s2
	s_add_u32 s18, s18, s1
	v_readlane_b32 s3, v254, 6
	s_nop 4
	s_mov_b32 s2, m0
	s_mov_b32 m0, s3
	s_nop 0
	global_load_lds_dwordx4 v142, s[14:15]
	s_mov_b32 m0, s2
	s_addc_u32 s19, s19, 0
	v_readlane_b32 s3, v254, 8
	s_nop 4
	s_mov_b32 s2, m0
	s_mov_b32 m0, s3
	s_nop 0
	global_load_lds_dwordx4 v142, s[16:17]
	s_mov_b32 m0, s2
	s_add_u32 s20, s20, s1
	v_readlane_b32 s3, v254, 10
	s_nop 4
	s_mov_b32 s2, m0
	s_mov_b32 m0, s3
	s_nop 0
	global_load_lds_dwordx4 v143, s[18:19]
	s_mov_b32 m0, s2
	s_addc_u32 s21, s21, 0
	v_readlane_b32 s3, v254, 12
	s_nop 4
	s_mov_b32 s2, m0
	s_mov_b32 m0, s3
	s_nop 0
	global_load_lds_dwordx4 v143, s[20:21]
	s_mov_b32 m0, s2
	s_cmpk_gt_i32 s82, 0x3ff
	s_cbranch_scc1 .LBB0_373
	s_add_u32 s2, s6, 0x8700000
	s_addc_u32 s3, s7, 0
	v_writelane_b32 v255, s2, 14
	s_add_u32 s2, s2, s4
	v_readlane_b32 s4, v254, 2
	v_writelane_b32 v255, s3, 15
	s_addc_u32 s3, s3, s5
	s_or_b32 s1, s1, s4
	s_add_u32 s1, s2, s1
	v_lshlrev_b32_e32 v0, 10, v2
	s_addc_u32 s2, s3, 0
	v_and_b32_e32 v6, 0x7c00, v0
	v_lshrrev_b32_e32 v0, 2, v3
	s_add_u32 s0, s1, s0
	v_and_b32_e32 v8, 8, v0
	s_addc_u32 s1, s2, 0
	v_lshlrev_b32_e32 v0, 1, v6
	v_lshl_add_u64 v[10:11], s[0:1], 0, v[0:1]
	v_lshlrev_b32_e32 v0, 1, v8
	v_lshl_add_u64 v[10:11], v[10:11], 0, v[0:1]
	global_load_dwordx4 v[66:69], v[10:11], off
	global_load_dwordx4 v[70:73], v[10:11], off offset:32
	global_load_dwordx4 v[74:77], v[10:11], off offset:64
	global_load_dwordx4 v[78:81], v[10:11], off offset:96
	v_and_b32_e32 v144, 31, v3
	v_lshlrev_b32_e32 v3, 8, v2
	v_lshlrev_b32_e32 v5, 3, v2
	s_movk_i32 s0, 0x3c18
	v_lshrrev_b32_e32 v0, 5, v2
	v_bitop3_b32 v3, v3, s0, v5 bitop3:0xc8
	v_lshlrev_b32_e32 v145, 1, v3
	v_lshlrev_b32_e32 v3, 10, v0
	v_lshlrev_b32_e32 v9, 4, v144
	v_readlane_b32 s0, v254, 4
	v_and_b32_e32 v7, 24, v5
	v_and_b32_e32 v4, 0xc0, v4
	v_add3_u32 v146, s0, v3, v9
	v_lshlrev_b32_e32 v3, 1, v2
	v_and_b32_e32 v3, 32, v3
	v_add3_u32 v3, s0, v3, v7
	v_cmp_eq_u32_e64 s[0:1], 0, v2
	v_lshlrev_b32_e32 v7, 8, v0
	v_add3_u32 v147, v3, v7, v4
	v_writelane_b32 v255, s0, 16
	s_waitcnt vmcnt(4)
	v_lshlrev_b32_e32 v148, 2, v0
	v_lshlrev_b32_e32 v0, 9, v0
	v_writelane_b32 v255, s1, 17
	v_lshlrev_b32_e32 v3, 1, v144
	v_readlane_b32 s0, v254, 16
	v_writelane_b32 v255, s92, 18
	v_cmp_ne_u32_e32 vcc, 0, v2
	v_add3_u32 v149, s0, v0, v3
	v_lshrrev_b32_e32 v3, 3, v2
	v_cmp_gt_u32_e64 s[8:9], 32, v2
	v_and_b32_e32 v0, 56, v5
	v_lshlrev_b32_e32 v7, 7, v3
	v_lshlrev_b32_e32 v2, 10, v3
	v_or_b32_e32 v4, 8, v3
	v_or_b32_e32 v10, 16, v3
	v_or_b32_e32 v3, 24, v3
	v_writelane_b32 v255, s93, 19
	v_lshl_add_u32 v5, v0, 1, s0
	v_lshlrev_b32_e32 v9, 7, v4
	v_lshlrev_b32_e32 v4, 10, v4
	v_lshlrev_b32_e32 v11, 7, v10
	v_lshlrev_b32_e32 v10, 10, v10
	s_waitcnt vmcnt(15)
	v_lshlrev_b32_e32 v13, 7, v3
	v_lshlrev_b32_e32 v12, 10, v3
	v_writelane_b32 v255, s94, 20
	s_xor_b64 s[76:77], vcc, -1
	v_lshlrev_b32_e32 v114, 1, v6
	v_lshlrev_b32_e32 v116, 1, v8
	v_lshlrev_b32_e32 v0, 1, v0
	v_add_u32_e32 v150, v5, v7
	v_lshlrev_b32_e32 v118, 1, v2
	v_add_u32_e32 v151, v5, v9
	v_lshlrev_b32_e32 v120, 1, v4
	v_add_u32_e32 v152, v5, v11
	v_lshlrev_b32_e32 v122, 1, v10
	v_add_u32_e32 v153, v5, v13
	v_lshlrev_b32_e32 v124, 1, v12
	s_mov_b32 s7, s82
	v_writelane_b32 v255, s95, 21
	s_waitcnt vmcnt(0)
	s_branch .LBB0_353

; #define LAS __attribute__((address_space(3)))
; __device__ __forceinline__ int crow(int r, int hi) { return (r & 3) + 8 * (r >> 2) + 4 * hi; }
; template <bool diag> __device__ __forceinline__ void sb_tile_math_t(f32x16& z0, f32x16& z1, float& carry, int s0, int tq, int hi) {
;     ...
;         for (int r = 0; r < 16; ++r) {
;             const int kv = s0 + crow(r, hi);
;             { float q = __builtin_amdgcn_rcpf(1.0f + __builtin_amdgcn_exp2f(z0[r])); if (diag && !(kv < tq)) q = 1.f; q0[r] = q; }
;             { float q = __builtin_amdgcn_rcpf(1.0f + __builtin_amdgcn_exp2f(z1[r])); if (diag && !(kv + 32 < tq)) q = 1.f; q1[r] = q; }
; __device__ __forceinline__ void sb_block_unit(bf16x8 (&qr)[4], int b, int hp  , int u  , int nb, int nhp, int nu, const bf16_t* Q, const bf16_t* K, const bf16_t* V, bf16_t* O, LAS char* L, int wid, int lane) {
;     const int r32 = lane & 31, hi = lane >> 5; const int hh = wid >> 2, qw = wid & 3, h = 2 * hp + hh;
;     const int t0 = 128 * u + 32 * qw; const size_t rowbase = (size_t)b * T; const int jtop = 2 * u + 1, jdw = t0 >> 6; const int tq = t0 + r32;
;     const bf16_t* Kh = K + rowbase * D + h * 64; const bf16_t* Vh = V + rowbase * D + h * 64;
;     const unsigned kvoff = (unsigned)lane * 2048u;
;     const unsigned vvoff = (unsigned)((lane >> 2) * D + (lane & 3) * 8) * 2u;
;     const int pa = 2 * qw, pb = 2 * qw + 1;
;     const bf16_t* Kwa = Kh + pa * 8; const bf16_t* Kwb = Kh + pb * 8;
;     const bf16_t* Vwa = Vh + (size_t)(16 * (pa & 3)) * D + (pa >> 2) * 32; const bf16_t* Vwb = Vh + (size_t)(16 * (pb & 3)) * D + (pb >> 2) * 32;
;     const unsigned hbase = (unsigned)(size_t)L + hh * SL_HEAD;
;     const unsigned kda = hbase + pa * 1024u, kdb = hbase + pb * 1024u, vda = hbase + SL_VOFF + pa * 1024u, vdb = hbase + SL_VOFF + pb * 1024u;
;     const LAS char* kp0 = L + hh * SL_HEAD + hi * 1024 + r32 * 16;
;     const LAS char* vp0 = L + hh * SL_HEAD + SL_VOFF + ((lane >> 4) & 1) * 32 + (lane & 3) * 8 + (4 * hi + ((lane & 15) >> 2)) * 64;
;     LAS unsigned* flags = (LAS unsigned*)(L + SL_FLAG);
;     if (lane == 0) flags[wid] = 0u;
;     ...
;     f32x16 o[2]; o[0] = f32x16{}; o[1] = f32x16{};
;     float carry = 1.f; bool gone = false;
;     asm volatile("s_waitcnt vmcnt(0) lgkmcnt(0)\n\ts_barrier" ::: "memory");
;     int sc = 0, sn = SL_SLOT, sn2 = 2 * SL_SLOT;
.LBB0_355:
	s_or_b64 exec, exec, s[4:5]
	s_and_b32 s0, s7, 31
	s_lshl_b32 s0, s0, 7
	v_readlane_b32 s3, v254, 13
	s_or_b32 s0, s3, s0
	s_and_b32 s2, s82, 31
	s_lshr_b32 s96, s0, 6
	s_ashr_i32 s0, s82, 8
	s_lshl_b32 s1, s2, 7
	s_or_b32 s11, s1, s3
	s_ashr_i32 s1, s0, 31
	s_lshl_b32 s2, s2, 1
	s_or_b32 s33, s2, 1
	s_lshr_b32 s97, s11, 6
	s_lshl_b64 s[12:13], s[0:1], 23
	v_readlane_b32 s0, v255, 10
	s_add_u32 s0, s0, s12
	v_readlane_b32 s1, v255, 11
	s_addc_u32 s1, s1, s13
	s_lshl_b32 s2, s82, 2
	s_and_b32 s2, s2, 0x380
	v_readlane_b32 s3, v254, 3
	s_add_i32 s2, s2, s3
	v_writelane_b32 v255, s2, 22
	s_lshl_b32 s2, s2, 1
	s_add_u32 s0, s0, s2
	s_addc_u32 s1, s1, 0
	v_readlane_b32 s3, v255, 12
	s_add_u32 s3, s3, s12
	v_readlane_b32 s4, v255, 13
	v_writelane_b32 v255, s12, 23
	s_addc_u32 s4, s4, s13
	s_add_u32 s5, s3, s2
	s_addc_u32 s4, s4, 0
	v_readlane_b32 s2, v254, 44
	s_add_u32 s83, s0, s2
	s_addc_u32 s80, s1, 0
	v_readlane_b32 s2, v254, 45
	s_add_u32 s3, s0, s2
	s_addc_u32 s78, s1, 0
	v_readlane_b32 s0, v254, 46
	s_add_u32 s0, s5, s0
	s_addc_u32 s1, s4, 0
	v_readlane_b32 s10, v254, 47
	s_add_u32 s2, s0, s10
	s_addc_u32 s6, s1, 0
	v_readlane_b32 s0, v254, 48
	s_add_u32 s0, s5, s0
	s_addc_u32 s1, s4, 0
	s_add_u32 s81, s0, s10
	s_addc_u32 s0, s1, 0
	s_and_b32 s1, s11, 0xfc0
	v_or_b32_e32 v3, s1, v148
	v_or_b32_e32 v2, s11, v144
	v_or_b32_e32 v4, 2, v3
	v_writelane_b32 v255, s13, 24
	v_cmp_lt_u32_e64 s[12:13], v4, v2
	v_or_b32_e32 v4, 3, v3
	v_or_b32_e32 v5, 1, v3
	v_cmp_lt_u32_e64 s[14:15], v4, v2
	v_cmp_lt_u32_e64 s[16:17], v5, v2
	v_or_b32_e32 v4, 34, v3
	v_or_b32_e32 v5, 32, v3
	v_or_b32_e32 v6, 35, v3
	v_or_b32_e32 v7, 33, v3
	v_cmp_lt_u32_e64 s[18:19], v4, v2
	v_cmp_lt_u32_e64 s[20:21], v5, v2
	v_cmp_lt_u32_e64 s[22:23], v6, v2
	v_or_b32_e32 v4, 10, v3
	v_or_b32_e32 v5, 8, v3
	v_or_b32_e32 v6, 11, v3
	v_cmp_lt_u32_e64 s[24:25], v7, v2
	v_or_b32_e32 v7, 9, v3
	v_cmp_lt_u32_e64 s[26:27], v4, v2
	v_cmp_lt_u32_e64 s[28:29], v5, v2
	v_cmp_lt_u32_e64 s[30:31], v6, v2
	v_or_b32_e32 v4, 42, v3
	v_or_b32_e32 v5, 40, v3
	v_or_b32_e32 v6, 43, v3
	v_cmp_lt_u32_e64 s[34:35], v7, v2
	v_or_b32_e32 v7, 41, v3
	v_cmp_lt_u32_e64 s[36:37], v4, v2
	v_cmp_lt_u32_e64 s[38:39], v5, v2
	v_cmp_lt_u32_e64 s[40:41], v6, v2
	v_or_b32_e32 v4, 18, v3
	v_or_b32_e32 v5, 16, v3
	v_or_b32_e32 v6, 19, v3
	v_cmp_lt_u32_e64 s[42:43], v7, v2
	v_or_b32_e32 v7, 17, v3
	v_cmp_lt_u32_e64 s[44:45], v4, v2
	v_cmp_lt_u32_e64 s[46:47], v5, v2
	v_cmp_lt_u32_e64 s[48:49], v6, v2
	v_or_b32_e32 v4, 50, v3
	v_or_b32_e32 v5, 48, v3
	v_or_b32_e32 v6, 51, v3
	v_cmp_lt_u32_e64 s[50:51], v7, v2
	v_or_b32_e32 v7, 49, v3
	v_cmp_lt_u32_e64 s[52:53], v4, v2
	v_cmp_lt_u32_e64 s[54:55], v5, v2
	v_cmp_lt_u32_e64 s[56:57], v6, v2
	v_or_b32_e32 v4, 26, v3
	v_or_b32_e32 v5, 24, v3
	v_or_b32_e32 v6, 27, v3
	s_waitcnt vmcnt(4) lgkmcnt(0)
	s_barrier
	v_writelane_b32 v255, s11, 25
	v_cmp_lt_u32_e64 s[10:11], v3, v2
	v_cmp_lt_u32_e64 s[58:59], v7, v2
	v_or_b32_e32 v7, 25, v3
	v_cmp_lt_u32_e64 s[60:61], v4, v2
	v_cmp_lt_u32_e64 s[62:63], v5, v2
	v_cmp_lt_u32_e64 s[64:65], v6, v2
	v_or_b32_e32 v4, 58, v3
	v_or_b32_e32 v5, 56, v3
	v_or_b32_e32 v6, 59, v3
	v_or_b32_e32 v3, 57, v3
	v_mov_b32_e32 v16, v1
	v_mov_b32_e32 v17, v1
	v_cmp_lt_u32_e64 s[66:67], v7, v2
	v_cmp_lt_u32_e64 s[68:69], v4, v2
	v_cmp_lt_u32_e64 s[70:71], v5, v2
	v_cmp_lt_u32_e64 s[72:73], v6, v2
	v_cmp_lt_u32_e64 s[74:75], v3, v2
	v_mov_b32_e32 v2, v1
	v_mov_b32_e32 v3, v1
	v_mov_b32_e32 v4, v1
	v_mov_b32_e32 v5, v1
	v_mov_b32_e32 v6, v1
	v_mov_b32_e32 v7, v1
	v_mov_b32_e32 v8, v1
	v_mov_b32_e32 v9, v1
	v_mov_b32_e32 v10, v1
	v_mov_b32_e32 v11, v1
	v_mov_b32_e32 v12, v1
	v_mov_b32_e32 v13, v1
	v_mov_b32_e32 v14, v1
	v_mov_b32_e32 v15, v1
	s_waitcnt vmcnt(12)
	v_mov_b64_e32 v[32:33], v[16:17]
	v_mov_b32_e32 v115, 1.0
	s_mov_b32 s84, 0x10000
	s_mov_b32 s79, 0x8000
	s_mov_b32 s88, 0
	v_mov_b64_e32 v[30:31], v[14:15]
	v_mov_b64_e32 v[28:29], v[12:13]
	v_mov_b64_e32 v[26:27], v[10:11]
	v_mov_b64_e32 v[24:25], v[8:9]
	v_mov_b64_e32 v[22:23], v[6:7]
	v_mov_b64_e32 v[20:21], v[4:5]
	v_mov_b64_e32 v[18:19], v[2:3]
	s_mov_b64 s[4:5], 0
